# DSA attention step loop hand-written: K/V of step s+2 requested during step s, V by LDS-DMA into two swizzled stages, 32-bit row offsets
# speedup vs baseline: 1.0188x; 1.0062x over previous
.LBB0_1123:
	s_or_b64 exec, exec, s[2:3]
	s_waitcnt lgkmcnt(0)
	v_add_u32_e32 v2, 31, v172
	v_and_b32_e32 v173, 15, v151
	v_ashrrev_i32_e32 v174, 4, v151
	v_ashrrev_i32_e32 v176, 5, v2
	v_mov_b32_e32 v29, 0
	v_lshlrev_b32_e32 v148, 7, v173
	v_mov_b32_e32 v149, v147
	v_cmp_lt_i32_e32 vcc, 0, v176
	v_lshlrev_b32_e32 v150, 2, v174
	v_mov_b32_e32 v28, v29
	v_mov_b32_e32 v27, v29
	v_mov_b32_e32 v26, v29
	v_mov_b32_e32 v33, v29
	v_mov_b32_e32 v32, v29
	v_mov_b32_e32 v31, v29
	v_mov_b32_e32 v30, v29
	v_mov_b32_e32 v25, v29
	v_mov_b32_e32 v24, v29
	v_mov_b32_e32 v23, v29
	v_mov_b32_e32 v22, v29
	v_mov_b32_e32 v21, v29
	v_mov_b32_e32 v20, v29
	v_mov_b32_e32 v19, v29
	v_mov_b32_e32 v18, v29
	v_mov_b32_e32 v17, v29
	v_mov_b32_e32 v16, v29
	v_mov_b32_e32 v15, v29
	v_mov_b32_e32 v14, v29
	v_mov_b32_e32 v13, v29
	v_mov_b32_e32 v12, v29
	v_mov_b32_e32 v11, v29
	v_mov_b32_e32 v10, v29
	v_mov_b32_e32 v9, v29
	v_mov_b32_e32 v8, v29
	v_mov_b32_e32 v7, v29
	v_mov_b32_e32 v6, v29
	v_mov_b32_e32 v5, v29
	v_mov_b32_e32 v4, v29
	v_mov_b32_e32 v3, v29
	v_mov_b32_e32 v2, v29
	v_mov_b32_e32 v179, v29
	s_and_saveexec_b64 s[0:1], vcc
	s_cbranch_execz .LBB0_1127
	v_readfirstlane_b32 s10, v176
	v_readfirstlane_b32 s36, v172
	v_readlane_b32 s37, v242, 49
	s_mul_i32 s5, s78, 0x3400000
	s_mul_hi_i32 s4, s78, 0x3400000
	s_add_u32 s2, s82, s5
	s_addc_u32 s3, s83, s4
	s_add_u32 s4, s2, 0x2800
	s_addc_u32 s5, s3, 0
	s_add_u32 s6, s2, 0x2900
	s_addc_u32 s7, s3, 0
	s_mul_i32 s20, s97, 0x3400
	s_mul_hi_u32 s21, s96, 0x3400
	s_add_i32 s21, s21, s20
	s_mul_i32 s20, s96, 0x3400
	s_add_u32 s20, s82, s20
	s_addc_u32 s21, s83, s21
	s_add_u32 s20, s20, 0x1800
	s_addc_u32 s21, s21, 0
	s_add_u32 s26, s89, 0x400
	s_lshl_b32 s27, s37, 13
	s_add_u32 s27, s27, 0x14000
	s_sub_u32 s37, s27, s26
	v_lshlrev_b32_e32 v152, 2, v150
	v_lshl_add_u32 v153, v148, 1, v152
	global_load_dwordx4 v[42:45], v153, s[20:21]
	global_load_dwordx4 v[34:37], v153, s[20:21] offset:64
	global_load_dwordx4 v[38:41], v153, s[20:21] offset:128
	global_load_dwordx4 v[46:49], v153, s[20:21] offset:192
	v_lshl_add_u32 v110, v173, 2, s89
	v_add_u32_e32 v111, s89, v150
	ds_read2_b32 v[98:99], v110 offset0:0 offset1:16
	ds_read2_b32 v[100:101], v111 offset0:0 offset1:4
	ds_read2_b32 v[102:103], v111 offset0:8 offset1:12
	ds_read2_b32 v[104:105], v111 offset0:16 offset1:20
	ds_read2_b32 v[106:107], v111 offset0:24 offset1:28
	v_lshlrev_b32_e32 v112, 1, v174
	v_xor_b32_e32 v112, v112, v173
	v_lshlrev_b32_e32 v177, 4, v112
	v_xor_b32_e32 v178, 0x80, v177
	v_lshrrev_b32_e32 v112, 2, v173
	v_add_u32_e32 v112, v112, v150
	v_and_b32_e32 v113, 7, v112
	v_and_b32_e32 v96, 3, v173
	v_lshlrev_b32_e32 v96, 3, v96
	v_lshl_add_u32 v112, v112, 8, v96
	v_add_u32_e32 v112, s26, v112
	v_xor_b32_e32 v96, 0, v113
	v_lshl_add_u32 v188, v96, 5, v112
	v_xor_b32_e32 v96, 1, v113
	v_lshl_add_u32 v189, v96, 5, v112
	v_xor_b32_e32 v96, 2, v113
	v_lshl_add_u32 v190, v96, 5, v112
	v_xor_b32_e32 v96, 3, v113
	v_lshl_add_u32 v191, v96, 5, v112
	v_xor_b32_e32 v96, 4, v113
	v_lshl_add_u32 v192, v96, 5, v112
	v_xor_b32_e32 v96, 5, v113
	v_lshl_add_u32 v193, v96, 5, v112
	v_xor_b32_e32 v96, 6, v113
	v_lshl_add_u32 v194, v96, 5, v112
	v_xor_b32_e32 v96, 7, v113
	v_lshl_add_u32 v195, v96, 5, v112
	v_add_u32_e32 v196, s37, v188
	v_add_u32_e32 v197, s37, v189
	v_add_u32_e32 v198, s37, v190
	v_add_u32_e32 v199, s37, v191
	v_add_u32_e32 v200, s37, v192
	v_add_u32_e32 v201, s37, v193
	v_add_u32_e32 v202, s37, v194
	v_add_u32_e32 v203, s37, v195
	v_mov_b32_e32 v2, 0
	v_mov_b32_e32 v3, 0
	v_mov_b32_e32 v4, 0
	v_mov_b32_e32 v5, 0
	v_mov_b32_e32 v6, 0
	v_mov_b32_e32 v7, 0
	v_mov_b32_e32 v8, 0
	v_mov_b32_e32 v9, 0
	v_mov_b32_e32 v10, 0
	v_mov_b32_e32 v11, 0
	v_mov_b32_e32 v12, 0
	v_mov_b32_e32 v13, 0
	v_mov_b32_e32 v14, 0
	v_mov_b32_e32 v15, 0
	v_mov_b32_e32 v16, 0
	v_mov_b32_e32 v17, 0
	v_mov_b32_e32 v18, 0
	v_mov_b32_e32 v19, 0
	v_mov_b32_e32 v20, 0
	v_mov_b32_e32 v21, 0
	v_mov_b32_e32 v22, 0
	v_mov_b32_e32 v23, 0
	v_mov_b32_e32 v24, 0
	v_mov_b32_e32 v25, 0
	v_mov_b32_e32 v26, 0
	v_mov_b32_e32 v27, 0
	v_mov_b32_e32 v28, 0
	v_mov_b32_e32 v29, 0
	v_mov_b32_e32 v30, 0
	v_mov_b32_e32 v31, 0
	v_mov_b32_e32 v32, 0
	v_mov_b32_e32 v33, 0
	v_mov_b32_e32 v179, 0
	v_mov_b32_e32 v181, 0xf149f2ca
	v_mov_b32_e32 v95, 0
	s_mov_b32 s11, 0
	s_mov_b32 s22, 0
	s_waitcnt lgkmcnt(0)
	v_mad_u32_u24 v108, v98, s35, v152
	v_mad_u32_u24 v109, v99, s35, v152
	global_load_dwordx4 v[50:53], v108, s[4:5]
	global_load_dwordx4 v[66:69], v109, s[4:5]
	global_load_dwordx4 v[54:57], v108, s[4:5] offset:64
	global_load_dwordx4 v[70:73], v109, s[4:5] offset:64
	global_load_dwordx4 v[58:61], v108, s[4:5] offset:128
	global_load_dwordx4 v[74:77], v109, s[4:5] offset:128
	global_load_dwordx4 v[62:65], v108, s[4:5] offset:192
	global_load_dwordx4 v[78:81], v109, s[4:5] offset:192
	s_mov_b32 m0, s26
	v_mad_u32_u24 v108, v100, s35, v177
	global_load_lds_dwordx4 v108, s[6:7]
	s_add_u32 m0, s26, 1024
	v_mad_u32_u24 v108, v101, s35, v178
	global_load_lds_dwordx4 v108, s[6:7]
	s_add_u32 m0, s26, 2048
	v_mad_u32_u24 v108, v102, s35, v177
	global_load_lds_dwordx4 v108, s[6:7]
	s_add_u32 m0, s26, 3072
	v_mad_u32_u24 v108, v103, s35, v178
	global_load_lds_dwordx4 v108, s[6:7]
	s_add_u32 m0, s26, 4096
	v_mad_u32_u24 v108, v104, s35, v177
	global_load_lds_dwordx4 v108, s[6:7]
	s_add_u32 m0, s26, 5120
	v_mad_u32_u24 v108, v105, s35, v178
	global_load_lds_dwordx4 v108, s[6:7]
	s_add_u32 m0, s26, 6144
	v_mad_u32_u24 v108, v106, s35, v177
	global_load_lds_dwordx4 v108, s[6:7]
	s_add_u32 m0, s26, 7168
	v_mad_u32_u24 v108, v107, s35, v178
	global_load_lds_dwordx4 v108, s[6:7]
	s_cmp_ge_u32 s10, 2
	s_cbranch_scc0 .Lat_A
	ds_read2_b32 v[98:99], v110 offset0:32 offset1:48
	ds_read2_b32 v[100:101], v111 offset0:32 offset1:36
	ds_read2_b32 v[102:103], v111 offset0:40 offset1:44
	ds_read2_b32 v[104:105], v111 offset0:48 offset1:52
	ds_read2_b32 v[106:107], v111 offset0:56 offset1:60
	s_waitcnt lgkmcnt(0)
	v_mad_u32_u24 v108, v98, s35, v152
	v_mad_u32_u24 v109, v99, s35, v152
	global_load_dwordx4 v[114:117], v108, s[4:5]
	global_load_dwordx4 v[130:133], v109, s[4:5]
	global_load_dwordx4 v[118:121], v108, s[4:5] offset:64
	global_load_dwordx4 v[134:137], v109, s[4:5] offset:64
	global_load_dwordx4 v[122:125], v108, s[4:5] offset:128
	global_load_dwordx4 v[138:141], v109, s[4:5] offset:128
	global_load_dwordx4 v[126:129], v108, s[4:5] offset:192
	global_load_dwordx4 v[142:145], v109, s[4:5] offset:192
	s_mov_b32 m0, s27
	v_mad_u32_u24 v108, v100, s35, v177
	global_load_lds_dwordx4 v108, s[6:7]
	s_add_u32 m0, s27, 1024
	v_mad_u32_u24 v108, v101, s35, v178
	global_load_lds_dwordx4 v108, s[6:7]
	s_add_u32 m0, s27, 2048
	v_mad_u32_u24 v108, v102, s35, v177
	global_load_lds_dwordx4 v108, s[6:7]
	s_add_u32 m0, s27, 3072
	v_mad_u32_u24 v108, v103, s35, v178
	global_load_lds_dwordx4 v108, s[6:7]
	s_add_u32 m0, s27, 4096
	v_mad_u32_u24 v108, v104, s35, v177
	global_load_lds_dwordx4 v108, s[6:7]
	s_add_u32 m0, s27, 5120
	v_mad_u32_u24 v108, v105, s35, v178
	global_load_lds_dwordx4 v108, s[6:7]
	s_add_u32 m0, s27, 6144
	v_mad_u32_u24 v108, v106, s35, v177
	global_load_lds_dwordx4 v108, s[6:7]
	s_add_u32 m0, s27, 7168
	v_mad_u32_u24 v108, v107, s35, v178
	global_load_lds_dwordx4 v108, s[6:7]
.Lat_A:
	s_sub_u32 s23, s10, s11
	s_cmp_ge_u32 s23, 3
	s_cbranch_scc0 .Lat_A_nosel
	ds_read2_b32 v[98:99], v110 offset0:64 offset1:80
	ds_read2_b32 v[100:101], v111 offset0:64 offset1:68
	ds_read2_b32 v[102:103], v111 offset0:72 offset1:76
	ds_read2_b32 v[104:105], v111 offset0:80 offset1:84
	ds_read2_b32 v[106:107], v111 offset0:88 offset1:92
.Lat_A_nosel:
	s_cmp_ge_u32 s23, 2
	s_cbranch_scc1 .Lat_A_k24
	s_waitcnt vmcnt(8)
	s_branch .Lat_A_qk
.Lat_A_k24:
	s_waitcnt vmcnt(24)
.Lat_A_qk:
	v_mfma_f32_16x16x32_bf16 v[82:85], v[50:53], v[42:45], 0
	v_mfma_f32_16x16x32_bf16 v[86:89], v[66:69], v[42:45], 0
	v_mfma_f32_16x16x32_bf16 v[82:85], v[54:57], v[34:37], v[82:85]
	v_mfma_f32_16x16x32_bf16 v[86:89], v[70:73], v[34:37], v[86:89]
	v_mfma_f32_16x16x32_bf16 v[82:85], v[58:61], v[38:41], v[82:85]
	v_mfma_f32_16x16x32_bf16 v[86:89], v[74:77], v[38:41], v[86:89]
	v_mfma_f32_16x16x32_bf16 v[82:85], v[62:65], v[46:49], v[82:85]
	v_mfma_f32_16x16x32_bf16 v[86:89], v[78:81], v[46:49], v[86:89]
	s_cmp_ge_u32 s23, 3
	s_cbranch_scc0 .Lat_A_nok
	s_waitcnt lgkmcnt(0)
	v_mad_u32_u24 v108, v98, s35, v152
	v_mad_u32_u24 v109, v99, s35, v152
	global_load_dwordx4 v[50:53], v108, s[4:5]
	global_load_dwordx4 v[66:69], v109, s[4:5]
	global_load_dwordx4 v[54:57], v108, s[4:5] offset:64
	global_load_dwordx4 v[70:73], v109, s[4:5] offset:64
	global_load_dwordx4 v[58:61], v108, s[4:5] offset:128
	global_load_dwordx4 v[74:77], v109, s[4:5] offset:128
	global_load_dwordx4 v[62:65], v108, s[4:5] offset:192
	global_load_dwordx4 v[78:81], v109, s[4:5] offset:192
.Lat_A_nok:
	v_add_u32_e32 v90, s22, v150
	v_add_u32_e32 v91, 16, v90
	s_add_u32 s24, s22, 32
	s_nop 6
	v_mul_f32_e32 v82, 0x3e0293ee, v82
	v_mul_f32_e32 v83, 0x3e0293ee, v83
	v_mul_f32_e32 v84, 0x3e0293ee, v84
	v_mul_f32_e32 v85, 0x3e0293ee, v85
	v_mul_f32_e32 v86, 0x3e0293ee, v86
	v_mul_f32_e32 v87, 0x3e0293ee, v87
	v_mul_f32_e32 v88, 0x3e0293ee, v88
	v_mul_f32_e32 v89, 0x3e0293ee, v89
	s_cmp_le_u32 s24, s36
	s_cbranch_scc1 .Lat_A_full
	v_add_u32_e32 v92, 0, v90
	v_cmp_lt_i32_e32 vcc, v92, v172
	v_add_u32_e32 v93, 0, v91
	s_nop 1
	v_cndmask_b32_e32 v82, v170, v82, vcc
	v_cmp_lt_i32_e32 vcc, v93, v172
	s_nop 1
	s_nop 0
	v_cndmask_b32_e32 v86, v170, v86, vcc
	v_add_u32_e32 v92, 1, v90
	v_cmp_lt_i32_e32 vcc, v92, v172
	v_add_u32_e32 v93, 1, v91
	s_nop 1
	v_cndmask_b32_e32 v83, v170, v83, vcc
	v_cmp_lt_i32_e32 vcc, v93, v172
	s_nop 1
	s_nop 0
	v_cndmask_b32_e32 v87, v170, v87, vcc
	v_add_u32_e32 v92, 2, v90
	v_cmp_lt_i32_e32 vcc, v92, v172
	v_add_u32_e32 v93, 2, v91
	s_nop 1
	v_cndmask_b32_e32 v84, v170, v84, vcc
	v_cmp_lt_i32_e32 vcc, v93, v172
	s_nop 1
	s_nop 0
	v_cndmask_b32_e32 v88, v170, v88, vcc
	v_add_u32_e32 v92, 3, v90
	v_cmp_lt_i32_e32 vcc, v92, v172
	v_add_u32_e32 v93, 3, v91
	s_nop 1
	v_cndmask_b32_e32 v85, v170, v85, vcc
	v_cmp_lt_i32_e32 vcc, v93, v172
	s_nop 1
	s_nop 0
	v_cndmask_b32_e32 v89, v170, v89, vcc
.Lat_A_full:
	v_max3_f32 v92, v82, v83, v84
	v_max3_f32 v93, v85, v86, v87
	v_max3_f32 v92, v92, v88, v89
	v_max_f32_e32 v92, v92, v93
	ds_bpermute_b32 v93, v161, v92
	s_waitcnt lgkmcnt(0)
	v_max_f32_e32 v92, v92, v93
	ds_bpermute_b32 v93, v162, v92
	s_waitcnt lgkmcnt(0)
	v_max3_f32 v180, v181, v92, v93
	v_sub_f32_e32 v94, v181, v180
	v_sub_f32_e32 v82, v82, v180
	v_sub_f32_e32 v83, v83, v180
	v_sub_f32_e32 v84, v84, v180
	v_sub_f32_e32 v85, v85, v180
	v_sub_f32_e32 v86, v86, v180
	v_sub_f32_e32 v87, v87, v180
	v_sub_f32_e32 v88, v88, v180
	v_sub_f32_e32 v89, v89, v180
	v_exp_f32_e32 v94, v94
	v_exp_f32_e32 v82, v82
	v_exp_f32_e32 v83, v83
	v_exp_f32_e32 v84, v84
	v_exp_f32_e32 v85, v85
	v_exp_f32_e32 v86, v86
	v_exp_f32_e32 v87, v87
	v_exp_f32_e32 v88, v88
	v_exp_f32_e32 v89, v89
	v_add_f32_e32 v92, v82, v83
	v_add_f32_e32 v93, v84, v85
	v_add_f32_e32 v97, v86, v87
	v_add_f32_e32 v92, v92, v93
	v_add_f32_e32 v96, v88, v89
	v_add_f32_e32 v97, v97, v96
	v_add_f32_e32 v92, v92, v97
	v_mov_b32_e32 v181, v180
	ds_bpermute_b32 v93, v161, v92
	v_cvt_pk_bf16_f32 v82, v82, v83
	v_cvt_pk_bf16_f32 v83, v84, v85
	v_cvt_pk_bf16_f32 v84, v86, v87
	v_cvt_pk_bf16_f32 v85, v88, v89
	v_pk_mul_f32 v[2:3], v[2:3], v[94:95] op_sel_hi:[1,0]
	v_pk_mul_f32 v[4:5], v[4:5], v[94:95] op_sel_hi:[1,0]
	v_pk_mul_f32 v[6:7], v[6:7], v[94:95] op_sel_hi:[1,0]
	v_pk_mul_f32 v[8:9], v[8:9], v[94:95] op_sel_hi:[1,0]
	v_pk_mul_f32 v[10:11], v[10:11], v[94:95] op_sel_hi:[1,0]
	v_pk_mul_f32 v[12:13], v[12:13], v[94:95] op_sel_hi:[1,0]
	v_pk_mul_f32 v[14:15], v[14:15], v[94:95] op_sel_hi:[1,0]
	v_pk_mul_f32 v[16:17], v[16:17], v[94:95] op_sel_hi:[1,0]
	s_waitcnt lgkmcnt(0)
	v_add_f32_e32 v92, v92, v93
	ds_bpermute_b32 v93, v162, v92
	v_pk_mul_f32 v[18:19], v[18:19], v[94:95] op_sel_hi:[1,0]
	v_pk_mul_f32 v[20:21], v[20:21], v[94:95] op_sel_hi:[1,0]
	v_pk_mul_f32 v[22:23], v[22:23], v[94:95] op_sel_hi:[1,0]
	v_pk_mul_f32 v[24:25], v[24:25], v[94:95] op_sel_hi:[1,0]
	v_pk_mul_f32 v[26:27], v[26:27], v[94:95] op_sel_hi:[1,0]
	v_pk_mul_f32 v[28:29], v[28:29], v[94:95] op_sel_hi:[1,0]
	v_pk_mul_f32 v[30:31], v[30:31], v[94:95] op_sel_hi:[1,0]
	v_pk_mul_f32 v[32:33], v[32:33], v[94:95] op_sel_hi:[1,0]
	s_cmp_ge_u32 s23, 3
	s_cbranch_scc1 .Lat_A_v24
	s_cmp_eq_u32 s23, 2
	s_cbranch_scc1 .Lat_A_v16
	s_waitcnt vmcnt(0)
	s_branch .Lat_A_pv
.Lat_A_v16:
	s_waitcnt vmcnt(16)
	s_branch .Lat_A_pv

.Lat_A_pv:
	s_waitcnt lgkmcnt(0)
	v_add_f32_e32 v92, v92, v93
	v_fma_f32 v179, v179, v94, v92
	ds_read_b64_tr_b16 v[86:87], v188
	ds_read_b64_tr_b16 v[88:89], v188 offset:4096
	ds_read_b64_tr_b16 v[244:245], v189
	ds_read_b64_tr_b16 v[246:247], v189 offset:4096
	s_waitcnt lgkmcnt(2)
	v_mfma_f32_16x16x32_bf16 v[2:5], v[86:89], v[82:85], v[2:5]
	ds_read_b64_tr_b16 v[86:87], v190
	ds_read_b64_tr_b16 v[88:89], v190 offset:4096
	s_waitcnt lgkmcnt(2)
	v_mfma_f32_16x16x32_bf16 v[6:9], v[244:247], v[82:85], v[6:9]
	ds_read_b64_tr_b16 v[244:245], v191
	ds_read_b64_tr_b16 v[246:247], v191 offset:4096
	s_waitcnt lgkmcnt(2)
	v_mfma_f32_16x16x32_bf16 v[10:13], v[86:89], v[82:85], v[10:13]
	ds_read_b64_tr_b16 v[86:87], v192
	ds_read_b64_tr_b16 v[88:89], v192 offset:4096
	s_waitcnt lgkmcnt(2)
	v_mfma_f32_16x16x32_bf16 v[14:17], v[244:247], v[82:85], v[14:17]
	ds_read_b64_tr_b16 v[244:245], v193
	ds_read_b64_tr_b16 v[246:247], v193 offset:4096
	s_waitcnt lgkmcnt(2)
	v_mfma_f32_16x16x32_bf16 v[18:21], v[86:89], v[82:85], v[18:21]
	ds_read_b64_tr_b16 v[86:87], v194
	ds_read_b64_tr_b16 v[88:89], v194 offset:4096
	s_waitcnt lgkmcnt(2)
	v_mfma_f32_16x16x32_bf16 v[22:25], v[244:247], v[82:85], v[22:25]
	ds_read_b64_tr_b16 v[244:245], v195
	ds_read_b64_tr_b16 v[246:247], v195 offset:4096
	s_waitcnt lgkmcnt(2)
	v_mfma_f32_16x16x32_bf16 v[30:33], v[86:89], v[82:85], v[30:33]
	s_waitcnt lgkmcnt(0)
	v_mfma_f32_16x16x32_bf16 v[26:29], v[244:247], v[82:85], v[26:29]
	s_cmp_ge_u32 s23, 3
	s_cbranch_scc0 .Lat_A_nov
	s_mov_b32 m0, s26
	v_mad_u32_u24 v108, v100, s35, v177
	global_load_lds_dwordx4 v108, s[6:7]
	s_add_u32 m0, s26, 1024
	v_mad_u32_u24 v108, v101, s35, v178
	global_load_lds_dwordx4 v108, s[6:7]
	s_add_u32 m0, s26, 2048
	v_mad_u32_u24 v108, v102, s35, v177
	global_load_lds_dwordx4 v108, s[6:7]
	s_add_u32 m0, s26, 3072
	v_mad_u32_u24 v108, v103, s35, v178
	global_load_lds_dwordx4 v108, s[6:7]
	s_add_u32 m0, s26, 4096
	v_mad_u32_u24 v108, v104, s35, v177
	global_load_lds_dwordx4 v108, s[6:7]
	s_add_u32 m0, s26, 5120
	v_mad_u32_u24 v108, v105, s35, v178
	global_load_lds_dwordx4 v108, s[6:7]
	s_add_u32 m0, s26, 6144
	v_mad_u32_u24 v108, v106, s35, v177
	global_load_lds_dwordx4 v108, s[6:7]
	s_add_u32 m0, s26, 7168
	v_mad_u32_u24 v108, v107, s35, v178
	global_load_lds_dwordx4 v108, s[6:7]
.Lat_A_nov:
	s_add_u32 s11, s11, 1
	s_add_u32 s22, s22, 32
	v_add_u32_e32 v110, 0x80, v110
	v_add_u32_e32 v111, 0x80, v111
	s_cmp_lt_u32 s11, s10
	s_cbranch_scc0 .Lat_done

.Lat_B_qk:
	v_mfma_f32_16x16x32_bf16 v[82:85], v[114:117], v[42:45], 0
	v_mfma_f32_16x16x32_bf16 v[86:89], v[130:133], v[42:45], 0
	v_mfma_f32_16x16x32_bf16 v[82:85], v[118:121], v[34:37], v[82:85]
	v_mfma_f32_16x16x32_bf16 v[86:89], v[134:137], v[34:37], v[86:89]
	v_mfma_f32_16x16x32_bf16 v[82:85], v[122:125], v[38:41], v[82:85]
	v_mfma_f32_16x16x32_bf16 v[86:89], v[138:141], v[38:41], v[86:89]
	v_mfma_f32_16x16x32_bf16 v[82:85], v[126:129], v[46:49], v[82:85]
	v_mfma_f32_16x16x32_bf16 v[86:89], v[142:145], v[46:49], v[86:89]
	s_cmp_ge_u32 s23, 3
	s_cbranch_scc0 .Lat_B_nok
	s_waitcnt lgkmcnt(0)
	v_mad_u32_u24 v108, v98, s35, v152
	v_mad_u32_u24 v109, v99, s35, v152
	global_load_dwordx4 v[114:117], v108, s[4:5]
	global_load_dwordx4 v[130:133], v109, s[4:5]
	global_load_dwordx4 v[118:121], v108, s[4:5] offset:64
	global_load_dwordx4 v[134:137], v109, s[4:5] offset:64
	global_load_dwordx4 v[122:125], v108, s[4:5] offset:128
	global_load_dwordx4 v[138:141], v109, s[4:5] offset:128
	global_load_dwordx4 v[126:129], v108, s[4:5] offset:192
	global_load_dwordx4 v[142:145], v109, s[4:5] offset:192

.Lat_B_pv:
	s_waitcnt lgkmcnt(0)
	v_add_f32_e32 v92, v92, v93
	v_fma_f32 v179, v179, v94, v92
	ds_read_b64_tr_b16 v[86:87], v196
	ds_read_b64_tr_b16 v[88:89], v196 offset:4096
	ds_read_b64_tr_b16 v[244:245], v197
	ds_read_b64_tr_b16 v[246:247], v197 offset:4096
	s_waitcnt lgkmcnt(2)
	v_mfma_f32_16x16x32_bf16 v[2:5], v[86:89], v[82:85], v[2:5]
	ds_read_b64_tr_b16 v[86:87], v198
	ds_read_b64_tr_b16 v[88:89], v198 offset:4096
	s_waitcnt lgkmcnt(2)
	v_mfma_f32_16x16x32_bf16 v[6:9], v[244:247], v[82:85], v[6:9]
	ds_read_b64_tr_b16 v[244:245], v199
	ds_read_b64_tr_b16 v[246:247], v199 offset:4096
	s_waitcnt lgkmcnt(2)
	v_mfma_f32_16x16x32_bf16 v[10:13], v[86:89], v[82:85], v[10:13]
	ds_read_b64_tr_b16 v[86:87], v200
	ds_read_b64_tr_b16 v[88:89], v200 offset:4096
	s_waitcnt lgkmcnt(2)
	v_mfma_f32_16x16x32_bf16 v[14:17], v[244:247], v[82:85], v[14:17]
	ds_read_b64_tr_b16 v[244:245], v201
	ds_read_b64_tr_b16 v[246:247], v201 offset:4096
	s_waitcnt lgkmcnt(2)
	v_mfma_f32_16x16x32_bf16 v[18:21], v[86:89], v[82:85], v[18:21]
	ds_read_b64_tr_b16 v[86:87], v202
	ds_read_b64_tr_b16 v[88:89], v202 offset:4096
	s_waitcnt lgkmcnt(2)
	v_mfma_f32_16x16x32_bf16 v[22:25], v[244:247], v[82:85], v[22:25]
	ds_read_b64_tr_b16 v[244:245], v203
	ds_read_b64_tr_b16 v[246:247], v203 offset:4096
	s_waitcnt lgkmcnt(2)
	v_mfma_f32_16x16x32_bf16 v[30:33], v[86:89], v[82:85], v[30:33]
	s_waitcnt lgkmcnt(0)
	v_mfma_f32_16x16x32_bf16 v[26:29], v[244:247], v[82:85], v[26:29]
	s_cmp_ge_u32 s23, 3
	s_cbranch_scc0 .Lat_B_nov
	s_mov_b32 m0, s27
	v_mad_u32_u24 v108, v100, s35, v177
	global_load_lds_dwordx4 v108, s[6:7]
	s_add_u32 m0, s27, 1024
	v_mad_u32_u24 v108, v101, s35, v178
	global_load_lds_dwordx4 v108, s[6:7]
	s_add_u32 m0, s27, 2048
	v_mad_u32_u24 v108, v102, s35, v177
	global_load_lds_dwordx4 v108, s[6:7]
	s_add_u32 m0, s27, 3072
	v_mad_u32_u24 v108, v103, s35, v178
	global_load_lds_dwordx4 v108, s[6:7]
	s_add_u32 m0, s27, 4096
	v_mad_u32_u24 v108, v104, s35, v177
	global_load_lds_dwordx4 v108, s[6:7]
	s_add_u32 m0, s27, 5120
	v_mad_u32_u24 v108, v105, s35, v178
	global_load_lds_dwordx4 v108, s[6:7]
	s_add_u32 m0, s27, 6144
	v_mad_u32_u24 v108, v106, s35, v177
	global_load_lds_dwordx4 v108, s[6:7]
	s_add_u32 m0, s27, 7168
	v_mad_u32_u24 v108, v107, s35, v178
	global_load_lds_dwordx4 v108, s[6:7]
.Lat_B_nov:
	s_add_u32 s11, s11, 1
	s_add_u32 s22, s22, 32
	v_add_u32_e32 v110, 0x80, v110
	v_add_u32_e32 v111, 0x80, v111
	s_cmp_lt_u32 s11, s10
	s_cbranch_scc1 .Lat_A
.Lat_done:
	s_nop 7
